# speedup vs baseline: 1.1370x; 1.0238x over previous
.LBB1_39:
	v_cmp_lt_u32_sdwa s[0:1], v45, v34 src0_sel:DWORD src1_sel:WORD_1
	s_nop 1
	v_cndmask_b32_e64 v26, 0, v45, s[0:1]
	v_add_u32_e32 v26, v26, v46
	global_load_ubyte v2, v26, s[62:63]
	v_cmp_lt_u32_sdwa s[4:5], v57, v34 src0_sel:DWORD src1_sel:WORD_1
	s_nop 1
	v_cndmask_b32_e64 v26, 0, v57, s[4:5]
	v_add_u32_e32 v26, v26, v46
	global_load_ubyte v10, v26, s[62:63]
	v_cmp_lt_u32_sdwa s[6:7], v56, v34 src0_sel:DWORD src1_sel:WORD_1
	s_nop 1
	v_cndmask_b32_e64 v26, 0, v56, s[6:7]
	v_add_u32_e32 v26, v26, v46
	global_load_ubyte v18, v26, s[62:63]
	v_cmp_lt_u32_sdwa s[8:9], v45, v35 src0_sel:DWORD src1_sel:WORD_1
	s_nop 1
	v_cndmask_b32_e64 v26, 0, v45, s[8:9]
	v_add_u32_e32 v26, v26, v47
	global_load_ubyte v3, v26, s[62:63]
	v_cmp_lt_u32_sdwa s[10:11], v57, v35 src0_sel:DWORD src1_sel:WORD_1
	s_nop 1
	v_cndmask_b32_e64 v26, 0, v57, s[10:11]
	v_add_u32_e32 v26, v26, v47
	global_load_ubyte v11, v26, s[62:63]
	v_cmp_lt_u32_sdwa s[12:13], v56, v35 src0_sel:DWORD src1_sel:WORD_1
	s_nop 1
	v_cndmask_b32_e64 v26, 0, v56, s[12:13]
	v_add_u32_e32 v26, v26, v47
	global_load_ubyte v19, v26, s[62:63]
	v_cmp_lt_u32_e64 s[14:15], v45, v38
	s_nop 1
	v_cndmask_b32_e64 v26, 0, v45, s[14:15]
	v_add_u32_e32 v26, v26, v48
	global_load_ubyte v4, v26, s[62:63]
	v_cmp_lt_u32_e64 s[16:17], v57, v38
	s_nop 1
	v_cndmask_b32_e64 v26, 0, v57, s[16:17]
	v_add_u32_e32 v26, v26, v48
	global_load_ubyte v12, v26, s[62:63]
	v_cmp_lt_u32_e64 s[18:19], v56, v38
	s_nop 1
	v_cndmask_b32_e64 v26, 0, v56, s[18:19]
	v_add_u32_e32 v26, v26, v48
	global_load_ubyte v20, v26, s[62:63]
	v_cmp_lt_u32_e64 s[22:23], v45, v39
	s_nop 1
	v_cndmask_b32_e64 v26, 0, v45, s[22:23]
	v_add_u32_e32 v26, v26, v49
	global_load_ubyte v5, v26, s[62:63]
	v_cmp_lt_u32_e64 s[24:25], v57, v39
	s_nop 1
	v_cndmask_b32_e64 v26, 0, v57, s[24:25]
	v_add_u32_e32 v26, v26, v49
	global_load_ubyte v13, v26, s[62:63]
	v_cmp_lt_u32_e64 s[26:27], v56, v39
	s_nop 1
	v_cndmask_b32_e64 v26, 0, v56, s[26:27]
	v_add_u32_e32 v26, v26, v49
	global_load_ubyte v21, v26, s[62:63]
	v_cmp_lt_u32_e64 s[28:29], v45, v40
	s_nop 1
	v_cndmask_b32_e64 v26, 0, v45, s[28:29]
	v_add_u32_e32 v26, v26, v50
	global_load_ubyte v6, v26, s[62:63]
	v_cmp_lt_u32_e64 s[30:31], v57, v40
	s_nop 1
	v_cndmask_b32_e64 v26, 0, v57, s[30:31]
	v_add_u32_e32 v26, v26, v50
	global_load_ubyte v14, v26, s[62:63]
	v_cmp_lt_u32_e64 s[32:33], v56, v40
	s_nop 1
	v_cndmask_b32_e64 v26, 0, v56, s[32:33]
	v_add_u32_e32 v26, v26, v50
	global_load_ubyte v22, v26, s[62:63]
	v_cmp_lt_u32_e64 s[34:35], v45, v41
	s_nop 1
	v_cndmask_b32_e64 v26, 0, v45, s[34:35]
	v_add_u32_e32 v26, v26, v51
	global_load_ubyte v7, v26, s[62:63]
	v_cmp_lt_u32_e64 s[36:37], v57, v41
	s_nop 1
	v_cndmask_b32_e64 v26, 0, v57, s[36:37]
	v_add_u32_e32 v26, v26, v51
	global_load_ubyte v15, v26, s[62:63]
	v_cmp_lt_u32_e64 s[40:41], v56, v41
	s_nop 1
	v_cndmask_b32_e64 v26, 0, v56, s[40:41]
	v_add_u32_e32 v26, v26, v51
	global_load_ubyte v23, v26, s[62:63]
	v_cmp_lt_u32_e64 s[42:43], v45, v42
	s_nop 1
	v_cndmask_b32_e64 v26, 0, v45, s[42:43]
	v_add_u32_e32 v26, v26, v52
	global_load_ubyte v8, v26, s[62:63]
	v_cmp_lt_u32_e64 s[44:45], v57, v42
	s_nop 1
	v_cndmask_b32_e64 v26, 0, v57, s[44:45]
	v_add_u32_e32 v26, v26, v52
	global_load_ubyte v16, v26, s[62:63]
	v_cmp_lt_u32_e64 s[46:47], v56, v42
	s_nop 1
	v_cndmask_b32_e64 v26, 0, v56, s[46:47]
	v_add_u32_e32 v26, v26, v52
	global_load_ubyte v24, v26, s[62:63]
	v_cmp_lt_u32_e64 s[48:49], v45, v43
	s_nop 1
	v_cndmask_b32_e64 v26, 0, v45, s[48:49]
	v_add_u32_e32 v26, v26, v53
	global_load_ubyte v9, v26, s[62:63]
	v_cmp_lt_u32_e64 s[50:51], v57, v43
	s_nop 1
	v_cndmask_b32_e64 v26, 0, v57, s[50:51]
	v_add_u32_e32 v26, v26, v53
	global_load_ubyte v17, v26, s[62:63]
	v_cmp_lt_u32_e64 s[52:53], v56, v43
	s_nop 1
	v_cndmask_b32_e64 v26, 0, v56, s[52:53]
	v_add_u32_e32 v26, v26, v53
	global_load_ubyte v25, v26, s[62:63]
	s_waitcnt vmcnt(23)
	v_cndmask_b32_e64 v2, -1, v2, s[0:1]
	s_waitcnt vmcnt(22)
	v_cndmask_b32_e64 v10, -1, v10, s[4:5]
	s_waitcnt vmcnt(21)
	v_cndmask_b32_e64 v18, -1, v18, s[6:7]
	s_waitcnt vmcnt(20)
	v_cndmask_b32_e64 v3, -1, v3, s[8:9]
	s_waitcnt vmcnt(19)
	v_cndmask_b32_e64 v11, -1, v11, s[10:11]
	s_waitcnt vmcnt(18)
	v_cndmask_b32_e64 v19, -1, v19, s[12:13]
	s_waitcnt vmcnt(17)
	v_cndmask_b32_e64 v4, -1, v4, s[14:15]
	s_waitcnt vmcnt(16)
	v_cndmask_b32_e64 v12, -1, v12, s[16:17]
	s_waitcnt vmcnt(15)
	v_cndmask_b32_e64 v20, -1, v20, s[18:19]
	s_waitcnt vmcnt(14)
	v_cndmask_b32_e64 v5, -1, v5, s[22:23]
	s_waitcnt vmcnt(13)
	v_cndmask_b32_e64 v13, -1, v13, s[24:25]
	s_waitcnt vmcnt(12)
	v_cndmask_b32_e64 v21, -1, v21, s[26:27]
	s_waitcnt vmcnt(11)
	v_cndmask_b32_e64 v6, -1, v6, s[28:29]
	s_waitcnt vmcnt(10)
	v_cndmask_b32_e64 v14, -1, v14, s[30:31]
	s_waitcnt vmcnt(9)
	v_cndmask_b32_e64 v22, -1, v22, s[32:33]
	s_waitcnt vmcnt(8)
	v_cndmask_b32_e64 v7, -1, v7, s[34:35]
	s_waitcnt vmcnt(7)
	v_cndmask_b32_e64 v15, -1, v15, s[36:37]
	s_waitcnt vmcnt(6)
	v_cndmask_b32_e64 v23, -1, v23, s[40:41]
	s_waitcnt vmcnt(5)
	v_cndmask_b32_e64 v8, -1, v8, s[42:43]
	s_waitcnt vmcnt(4)
	v_cndmask_b32_e64 v16, -1, v16, s[44:45]
	s_waitcnt vmcnt(3)
	v_cndmask_b32_e64 v24, -1, v24, s[46:47]
	s_waitcnt vmcnt(2)
	v_cndmask_b32_e64 v9, -1, v9, s[48:49]
	s_waitcnt vmcnt(1)
	v_cndmask_b32_e64 v17, -1, v17, s[50:51]
	s_waitcnt vmcnt(0)
	v_cndmask_b32_e64 v25, -1, v25, s[52:53]
	s_or_b64 exec, exec, s[20:21]
	v_cmp_ne_u32_e64 s[0:1], -1, v2
	s_and_saveexec_b64 s[4:5], s[0:1]
	s_cbranch_execz .LBB1_15

.LBB2_29:
	v_cmp_lt_u32_sdwa s[0:1], v19, v8 src0_sel:DWORD src1_sel:WORD_1
	v_add_u32_e32 v42, 8, v19
	v_cmp_lt_u32_sdwa s[30:31], v42, v8 src0_sel:DWORD src1_sel:WORD_1
	v_cndmask_b32_e64 v2, 0, v19, s[0:1]
	v_add_u32_e32 v2, v2, v20
	v_lshl_add_u64 v[26:27], v[2:3], 2, s[60:61]
	v_cndmask_b32_e64 v2, 0, v42, s[30:31]
	v_add_u32_e32 v43, 16, v19
	v_add_u32_e32 v2, v2, v20
	v_cmp_lt_u32_sdwa s[4:5], v43, v8 src0_sel:DWORD src1_sel:WORD_1
	v_lshl_add_u64 v[28:29], v[2:3], 2, s[60:61]
	v_cmp_lt_u32_sdwa s[6:7], v19, v9 src0_sel:DWORD src1_sel:WORD_1
	v_cndmask_b32_e64 v2, 0, v43, s[4:5]
	v_add_u32_e32 v2, v2, v20
	v_lshl_add_u64 v[30:31], v[2:3], 2, s[60:61]
	v_cndmask_b32_e64 v2, 0, v19, s[6:7]
	v_add_u32_e32 v2, v2, v21
	v_cmp_lt_u32_sdwa s[8:9], v42, v9 src0_sel:DWORD src1_sel:WORD_1
	v_lshl_add_u64 v[32:33], v[2:3], 2, s[60:61]
	v_cmp_lt_u32_sdwa s[10:11], v43, v9 src0_sel:DWORD src1_sel:WORD_1
	v_cndmask_b32_e64 v2, 0, v42, s[8:9]
	v_add_u32_e32 v2, v2, v21
	v_lshl_add_u64 v[34:35], v[2:3], 2, s[60:61]
	v_cndmask_b32_e64 v2, 0, v43, s[10:11]
	v_add_u32_e32 v2, v2, v21
	v_cmp_lt_u32_e64 s[12:13], v19, v7
	v_lshl_add_u64 v[36:37], v[2:3], 2, s[60:61]
	v_cmp_lt_u32_e64 s[14:15], v42, v7
	v_cndmask_b32_e64 v2, 0, v19, s[12:13]
	v_add_u32_e32 v2, v2, v22
	v_lshl_add_u64 v[38:39], v[2:3], 2, s[60:61]
	v_cndmask_b32_e64 v2, 0, v42, s[14:15]
	v_add_u32_e32 v2, v2, v22
	v_cmp_lt_u32_e64 s[16:17], v43, v7
	v_lshl_add_u64 v[40:41], v[2:3], 2, s[60:61]
	v_cmp_lt_u32_e64 s[18:19], v19, v13
	v_cndmask_b32_e64 v2, 0, v43, s[16:17]
	v_add_u32_e32 v2, v2, v22
	global_load_dword v44, v[26:27], off
	global_load_dword v45, v[28:29], off
	global_load_dword v46, v[30:31], off
	global_load_dword v47, v[32:33], off
	s_waitcnt lgkmcnt(5)
	global_load_dword v49, v[34:35], off
	s_waitcnt lgkmcnt(4)
	global_load_dword v50, v[36:37], off
	global_load_dword v51, v[38:39], off
	global_load_dword v52, v[40:41], off
	v_lshl_add_u64 v[26:27], v[2:3], 2, s[60:61]
	v_cndmask_b32_e64 v2, 0, v19, s[18:19]
	v_add_u32_e32 v2, v2, v23
	v_cmp_lt_u32_e64 s[20:21], v42, v13
	v_lshl_add_u64 v[28:29], v[2:3], 2, s[60:61]
	v_cmp_lt_u32_e64 s[22:23], v43, v13
	v_cndmask_b32_e64 v2, 0, v42, s[20:21]
	v_add_u32_e32 v2, v2, v23
	v_lshl_add_u64 v[30:31], v[2:3], 2, s[60:61]
	v_cndmask_b32_e64 v2, 0, v43, s[22:23]
	v_add_u32_e32 v2, v2, v23
	v_cmp_lt_u32_e64 s[24:25], v19, v14
	v_lshl_add_u64 v[32:33], v[2:3], 2, s[60:61]
	v_cmp_lt_u32_e64 s[26:27], v42, v14
	v_cndmask_b32_e64 v2, 0, v19, s[24:25]
	v_add_u32_e32 v2, v2, v4
	v_lshl_add_u64 v[34:35], v[2:3], 2, s[60:61]
	v_cndmask_b32_e64 v2, 0, v42, s[26:27]
	v_add_u32_e32 v2, v2, v4
	v_cmp_lt_u32_e64 s[28:29], v43, v14
	v_lshl_add_u64 v[36:37], v[2:3], 2, s[60:61]
	v_cmp_lt_u32_e64 s[34:35], v19, v15
	v_cndmask_b32_e64 v2, 0, v43, s[28:29]
	v_add_u32_e32 v2, v2, v4
	v_lshl_add_u64 v[38:39], v[2:3], 2, s[60:61]
	v_cndmask_b32_e64 v2, 0, v19, s[34:35]
	v_add_u32_e32 v2, v2, v5
	v_cmp_lt_u32_e64 s[36:37], v42, v15
	v_lshl_add_u64 v[40:41], v[2:3], 2, s[60:61]
	v_cmp_lt_u32_e64 s[38:39], v43, v15
	v_cndmask_b32_e64 v2, 0, v42, s[36:37]
	v_add_u32_e32 v2, v2, v5
	s_waitcnt lgkmcnt(1)
	global_load_dword v53, v[26:27], off
	global_load_dword v54, v[28:29], off
	s_waitcnt lgkmcnt(0)
	global_load_dword v55, v[30:31], off
	global_load_dword v56, v[32:33], off
	global_load_dword v57, v[34:35], off
	global_load_dword v58, v[36:37], off
	global_load_dword v59, v[38:39], off
	global_load_dword v60, v[40:41], off
	v_lshl_add_u64 v[26:27], v[2:3], 2, s[60:61]
	v_cndmask_b32_e64 v2, 0, v43, s[38:39]
	v_add_u32_e32 v2, v2, v5
	v_cmp_lt_u32_e64 s[40:41], v19, v16
	v_lshl_add_u64 v[28:29], v[2:3], 2, s[60:61]
	v_cmp_lt_u32_e64 s[42:43], v42, v16
	v_cndmask_b32_e64 v2, 0, v19, s[40:41]
	v_add_u32_e32 v2, v2, v10
	v_lshl_add_u64 v[30:31], v[2:3], 2, s[60:61]
	v_cndmask_b32_e64 v2, 0, v42, s[42:43]
	v_add_u32_e32 v2, v2, v10
	v_cmp_lt_u32_e64 s[44:45], v43, v16
	v_lshl_add_u64 v[32:33], v[2:3], 2, s[60:61]
	v_cmp_lt_u32_e64 s[46:47], v19, v17
	v_cndmask_b32_e64 v2, 0, v43, s[44:45]
	v_add_u32_e32 v2, v2, v10
	v_lshl_add_u64 v[34:35], v[2:3], 2, s[60:61]
	v_cndmask_b32_e64 v2, 0, v19, s[46:47]
	v_add_u32_e32 v2, v2, v11
	v_cmp_lt_u32_e64 s[48:49], v42, v17
	v_lshl_add_u64 v[36:37], v[2:3], 2, s[60:61]
	v_cmp_lt_u32_e64 s[50:51], v43, v17
	v_cndmask_b32_e64 v2, 0, v42, s[48:49]
	v_add_u32_e32 v2, v2, v11
	v_lshl_add_u64 v[38:39], v[2:3], 2, s[60:61]
	v_cndmask_b32_e64 v2, 0, v43, s[50:51]
	v_add_u32_e32 v2, v2, v11
	v_lshl_add_u64 v[40:41], v[2:3], 2, s[60:61]
	global_load_dword v2, v[26:27], off
	s_nop 0
	global_load_dword v26, v[28:29], off
	global_load_dword v42, v[30:31], off
	s_nop 0
	global_load_dword v33, v[32:33], off
	s_nop 0
	global_load_dword v61, v[34:35], off
	global_load_dword v62, v[36:37], off
	global_load_dword v63, v[38:39], off
	global_load_dword v64, v[40:41], off
	s_waitcnt vmcnt(23)
	v_cndmask_b32_e64 v48, -1, v44, s[0:1]
	s_waitcnt vmcnt(22)
	v_cndmask_b32_e64 v40, -1, v45, s[30:31]
	s_waitcnt vmcnt(21)
	v_cndmask_b32_e64 v32, -1, v46, s[4:5]
	s_waitcnt vmcnt(20)
	v_cndmask_b32_e64 v47, -1, v47, s[6:7]
	s_waitcnt vmcnt(19)
	v_cndmask_b32_e64 v39, -1, v49, s[8:9]
	s_waitcnt vmcnt(18)
	v_cndmask_b32_e64 v31, -1, v50, s[10:11]
	v_and_b32_e32 v50, 0xffff, v47
	s_waitcnt vmcnt(17)
	v_cndmask_b32_e64 v46, -1, v51, s[12:13]
	s_waitcnt vmcnt(16)
	v_cndmask_b32_e64 v38, -1, v52, s[14:15]
	v_cmp_eq_u32_e64 s[0:1], -1, v46
	v_cmp_eq_u32_e64 s[12:13], -1, v40
	v_cmp_eq_u32_e64 s[14:15], -1, v39
	v_and_b32_e32 v49, 0xffff, v48
	v_bfe_u32 v70, v48, 16, 7
	s_waitcnt vmcnt(15)
	v_cndmask_b32_e64 v30, -1, v53, s[16:17]
	s_waitcnt vmcnt(14)
	v_cndmask_b32_e64 v45, -1, v54, s[18:19]
	v_cmp_eq_u32_e64 s[18:19], -1, v47
	s_waitcnt vmcnt(12)
	v_cndmask_b32_e64 v29, -1, v56, s[22:23]
	s_waitcnt vmcnt(11)
	v_cndmask_b32_e64 v44, -1, v57, s[24:25]
	v_cndmask_b32_e64 v50, v50, 0, s[18:19]
	v_lshlrev_b32_e32 v52, 3, v50
	v_and_b32_e32 v50, 0xffff, v46
	v_cndmask_b32_e64 v50, v50, 0, s[0:1]
	v_lshlrev_b32_e32 v54, 3, v50
	v_and_b32_e32 v50, 0xffff, v45
	v_cmp_eq_u32_e64 s[4:5], -1, v44
	s_waitcnt vmcnt(8)
	v_cndmask_b32_e64 v43, -1, v60, s[34:35]
	v_cndmask_b32_e64 v36, -1, v58, s[26:27]
	v_cmp_eq_u32_e64 s[6:7], -1, v43
	v_cndmask_b32_e64 v37, -1, v55, s[20:21]
	v_cmp_eq_u32_e64 s[20:21], -1, v48
	v_cndmask_b32_e64 v28, -1, v59, s[28:29]
	v_cmp_eq_u32_e64 s[16:17], -1, v38
	v_cndmask_b32_e64 v49, v49, 0, s[20:21]
	v_and_b32_e32 v55, 0xffff, v36
	v_cmp_eq_u32_e64 s[34:35], -1, v30
	v_lshlrev_b32_e32 v49, 3, v49
	v_and_b32_e32 v65, 0xffff, v29
	v_cmp_eq_u32_e64 s[30:31], -1, v29
	v_cmp_eq_u32_e64 s[28:29], -1, v28
	v_cndmask_b32_e64 v70, v70, v24, s[20:21]
	v_cndmask_b32_e64 v65, v65, 0, s[30:31]
	v_lshlrev_b32_e32 v81, 3, v65
	s_waitcnt vmcnt(7)
	v_cndmask_b32_e64 v35, -1, v2, s[36:37]
	s_waitcnt vmcnt(6)
	v_cndmask_b32_e64 v27, -1, v26, s[38:39]
	s_waitcnt vmcnt(5)
	v_cndmask_b32_e64 v42, -1, v42, s[40:41]
	v_cmp_eq_u32_e64 s[8:9], -1, v42
	s_waitcnt vmcnt(4)
	v_cndmask_b32_e64 v34, -1, v33, s[42:43]
	s_waitcnt vmcnt(2)
	v_cndmask_b32_e64 v41, -1, v62, s[46:47]
	v_cmp_eq_u32_e64 s[10:11], -1, v41
	s_waitcnt vmcnt(0)
	v_cndmask_b32_e64 v2, -1, v64, s[50:51]
	v_cmp_eq_u32_e64 s[50:51], -1, v45
	v_cndmask_b32_e64 v33, -1, v63, s[48:49]
	v_cmp_eq_u32_e64 s[46:47], -1, v36
	v_cndmask_b32_e64 v50, v50, 0, s[50:51]
	v_lshlrev_b32_e32 v56, 3, v50
	v_and_b32_e32 v50, 0xffff, v44
	v_cndmask_b32_e64 v50, v50, 0, s[4:5]
	v_lshlrev_b32_e32 v58, 3, v50
	v_and_b32_e32 v50, 0xffff, v43
	v_cndmask_b32_e64 v50, v50, 0, s[6:7]
	v_lshlrev_b32_e32 v60, 3, v50
	v_and_b32_e32 v50, 0xffff, v42
	v_cndmask_b32_e64 v50, v50, 0, s[8:9]
	v_lshlrev_b32_e32 v62, 3, v50
	v_and_b32_e32 v50, 0xffff, v41
	v_cndmask_b32_e64 v50, v50, 0, s[10:11]
	v_lshlrev_b32_e32 v64, 3, v50
	v_and_b32_e32 v50, 0xffff, v40
	v_cndmask_b32_e64 v50, v50, 0, s[12:13]
	v_lshlrev_b32_e32 v66, 3, v50
	v_and_b32_e32 v50, 0xffff, v39
	v_cndmask_b32_e64 v50, v50, 0, s[14:15]
	v_lshlrev_b32_e32 v68, 3, v50
	v_and_b32_e32 v50, 0xffff, v38
	v_and_b32_e32 v59, 0xffff, v33
	v_cmp_eq_u32_e64 s[40:41], -1, v33
	v_and_b32_e32 v63, 0xffff, v30
	v_cndmask_b32_e64 v53, v50, 0, s[16:17]
	v_cndmask_b32_e64 v55, v55, 0, s[46:47]
	v_cndmask_b32_e64 v59, v59, 0, s[40:41]
	v_cndmask_b32_e64 v63, v63, 0, s[34:35]
	global_load_dwordx2 v[50:51], v49, s[58:59]
	v_cmp_eq_u32_e64 s[48:49], -1, v37
	v_lshlrev_b32_e32 v74, 3, v55
	global_load_dwordx2 v[54:55], v54, s[58:59]
	v_lshlrev_b32_e32 v77, 3, v59
	global_load_dwordx2 v[58:59], v58, s[58:59]
	v_lshlrev_b32_e32 v80, 3, v63
	global_load_dwordx2 v[62:63], v62, s[58:59]
	v_lshlrev_b32_e32 v49, 3, v53
	v_and_b32_e32 v53, 0xffff, v37
	v_cndmask_b32_e64 v53, v53, 0, s[48:49]
	v_lshlrev_b32_e32 v72, 3, v53
	global_load_dwordx2 v[52:53], v52, s[58:59]
	v_cndmask_b32_e64 v26, -1, v61, s[44:45]
	v_and_b32_e32 v57, 0xffff, v35
	v_cmp_eq_u32_e64 s[44:45], -1, v35
	v_cmp_eq_u32_e64 s[42:43], -1, v34
	v_and_b32_e32 v61, 0xffff, v32
	v_cndmask_b32_e64 v57, v57, 0, s[44:45]
	v_lshlrev_b32_e32 v75, 3, v57
	v_and_b32_e32 v57, 0xffff, v34
	v_cndmask_b32_e64 v57, v57, 0, s[42:43]
	v_lshlrev_b32_e32 v76, 3, v57
	global_load_dwordx2 v[56:57], v56, s[58:59]
	v_cmp_eq_u32_e64 s[38:39], -1, v32
	v_cmp_eq_u32_e64 s[36:37], -1, v31
	v_and_b32_e32 v65, 0xffff, v28
	v_cndmask_b32_e64 v61, v61, 0, s[38:39]
	v_lshlrev_b32_e32 v78, 3, v61
	v_and_b32_e32 v61, 0xffff, v31
	v_cndmask_b32_e64 v61, v61, 0, s[36:37]
	v_lshlrev_b32_e32 v79, 3, v61
	global_load_dwordx2 v[60:61], v60, s[58:59]
	v_cndmask_b32_e64 v65, v65, 0, s[28:29]
	v_lshlrev_b32_e32 v82, 3, v65
	global_load_dwordx2 v[64:65], v64, s[58:59]
	v_and_b32_e32 v67, 0xffff, v27
	v_cmp_eq_u32_e64 s[26:27], -1, v27
	v_and_b32_e32 v69, 0xffff, v26
	v_cmp_eq_u32_e64 s[24:25], -1, v26
	v_cndmask_b32_e64 v67, v67, 0, s[26:27]
	v_lshlrev_b32_e32 v83, 3, v67
	global_load_dwordx2 v[66:67], v66, s[58:59]
	v_cndmask_b32_e64 v69, v69, 0, s[24:25]
	v_lshlrev_b32_e32 v84, 3, v69
	v_and_b32_e32 v69, 0xffff, v2
	v_cmp_eq_u32_e64 s[22:23], -1, v2
	v_lshlrev_b32_e32 v91, 2, v70
	v_cmp_ne_u32_e64 s[20:21], -1, v35
	v_cndmask_b32_e64 v69, v69, 0, s[22:23]
	v_lshlrev_b32_e32 v85, 3, v69
	global_load_dwordx2 v[68:69], v68, s[58:59]
	s_nop 0
	global_load_dwordx2 v[70:71], v49, s[58:59]
	s_nop 0
	global_load_dwordx2 v[72:73], v72, s[58:59]
	s_nop 0
	global_load_dwordx2 v[98:99], v74, s[58:59]
	global_load_dwordx2 v[100:101], v75, s[58:59]
	global_load_dwordx2 v[102:103], v76, s[58:59]
	global_load_dwordx2 v[104:105], v77, s[58:59]
	global_load_dwordx2 v[106:107], v78, s[58:59]
	global_load_dwordx2 v[108:109], v79, s[58:59]
	global_load_dwordx2 v[110:111], v80, s[58:59]
	global_load_dwordx2 v[112:113], v81, s[58:59]
	global_load_dwordx2 v[114:115], v82, s[58:59]
	global_load_dwordx2 v[116:117], v83, s[58:59]
	global_load_dwordx2 v[118:119], v84, s[58:59]
	global_load_dwordx2 v[120:121], v85, s[58:59]
	v_bfe_u32 v49, v47, 16, 7
	s_waitcnt vmcnt(23)
	ds_add_u32 v91, v50 offset:1024
	ds_add_u32 v91, v51 offset:1792
	v_cndmask_b32_e64 v49, v49, v24, s[18:19]
	v_lshlrev_b32_e32 v49, 2, v49
	ds_add_rtn_u32 v96, v91, v25 offset:2560
	s_waitcnt vmcnt(19)
	s_cmp_eq_u64 s[18:19], exec
	s_cbranch_scc1 .Lcsk_0
	ds_add_u32 v49, v52 offset:1024
	ds_add_u32 v49, v53 offset:1792
	ds_add_rtn_u32 v94, v49, v25 offset:2560
	ds_read_b32 v95, v49 offset:3328
.Lcsk_0:
	v_bfe_u32 v49, v46, 16, 7
	v_cndmask_b32_e64 v49, v49, v24, s[0:1]
	v_lshlrev_b32_e32 v49, 2, v49
	s_cmp_eq_u64 s[0:1], exec
	s_cbranch_scc1 .Lcsk_1
	ds_add_u32 v49, v54 offset:1024
	ds_add_u32 v49, v55 offset:1792
	ds_add_rtn_u32 v92, v49, v25 offset:2560
	ds_read_b32 v93, v49 offset:3328
.Lcsk_1:
	v_bfe_u32 v49, v45, 16, 7
	v_cndmask_b32_e64 v49, v49, v24, s[50:51]
	v_lshlrev_b32_e32 v49, 2, v49
	s_waitcnt vmcnt(18)
	s_cmp_eq_u64 s[50:51], exec
	s_cbranch_scc1 .Lcsk_2
	ds_add_u32 v49, v56 offset:1024
	ds_add_u32 v49, v57 offset:1792
	ds_add_rtn_u32 v89, v49, v25 offset:2560
	ds_read_b32 v90, v49 offset:3328
.Lcsk_2:
	v_bfe_u32 v49, v44, 16, 7
	v_cndmask_b32_e64 v49, v49, v24, s[4:5]
	v_lshlrev_b32_e32 v49, 2, v49
	s_cmp_eq_u64 s[4:5], exec
	s_cbranch_scc1 .Lcsk_3
	ds_add_u32 v49, v58 offset:1024
	ds_add_u32 v49, v59 offset:1792
	ds_add_rtn_u32 v87, v49, v25 offset:2560
	ds_read_b32 v88, v49 offset:3328
.Lcsk_3:
	v_bfe_u32 v49, v43, 16, 7
	v_cndmask_b32_e64 v49, v49, v24, s[6:7]
	v_lshlrev_b32_e32 v49, 2, v49
	s_waitcnt vmcnt(17)
	s_cmp_eq_u64 s[6:7], exec
	s_cbranch_scc1 .Lcsk_4
	ds_add_u32 v49, v60 offset:1024
	ds_add_u32 v49, v61 offset:1792
	ds_add_rtn_u32 v85, v49, v25 offset:2560
	ds_read_b32 v86, v49 offset:3328
.Lcsk_4:
	v_bfe_u32 v49, v42, 16, 7
	v_cndmask_b32_e64 v49, v49, v24, s[8:9]
	v_lshlrev_b32_e32 v49, 2, v49
	s_cmp_eq_u64 s[8:9], exec
	s_cbranch_scc1 .Lcsk_5
	ds_add_u32 v49, v62 offset:1024
	ds_add_u32 v49, v63 offset:1792
	ds_add_rtn_u32 v83, v49, v25 offset:2560
	ds_read_b32 v84, v49 offset:3328
.Lcsk_5:
	v_bfe_u32 v49, v41, 16, 7
	v_cndmask_b32_e64 v49, v49, v24, s[10:11]
	v_lshlrev_b32_e32 v49, 2, v49
	s_waitcnt vmcnt(16)
	s_cmp_eq_u64 s[10:11], exec
	s_cbranch_scc1 .Lcsk_6
	ds_add_u32 v49, v64 offset:1024
	ds_add_u32 v49, v65 offset:1792
	ds_add_rtn_u32 v81, v49, v25 offset:2560
	ds_read_b32 v82, v49 offset:3328
.Lcsk_6:
	v_bfe_u32 v49, v40, 16, 7
	v_cndmask_b32_e64 v49, v49, v24, s[12:13]
	v_lshlrev_b32_e32 v49, 2, v49
	s_waitcnt vmcnt(15)
	s_cmp_eq_u64 s[12:13], exec
	s_cbranch_scc1 .Lcsk_7
	ds_add_u32 v49, v66 offset:1024
	ds_add_u32 v49, v67 offset:1792
	ds_add_rtn_u32 v79, v49, v25 offset:2560
	ds_read_b32 v80, v49 offset:3328
.Lcsk_7:
	v_bfe_u32 v49, v39, 16, 7
	v_cndmask_b32_e64 v49, v49, v24, s[14:15]
	v_lshlrev_b32_e32 v49, 2, v49
	s_waitcnt vmcnt(14)
	s_cmp_eq_u64 s[14:15], exec
	s_cbranch_scc1 .Lcsk_8
	ds_add_u32 v49, v68 offset:1024
	ds_add_u32 v49, v69 offset:1792
	ds_add_rtn_u32 v77, v49, v25 offset:2560
	ds_read_b32 v78, v49 offset:3328
.Lcsk_8:
	v_bfe_u32 v49, v38, 16, 7
	v_cndmask_b32_e64 v49, v49, v24, s[16:17]
	v_lshlrev_b32_e32 v49, 2, v49
	s_waitcnt vmcnt(13)
	s_cmp_eq_u64 s[16:17], exec
	s_cbranch_scc1 .Lcsk_9
	ds_add_u32 v49, v70 offset:1024
	ds_add_u32 v49, v71 offset:1792
	ds_add_rtn_u32 v75, v49, v25 offset:2560
	ds_read_b32 v76, v49 offset:3328
.Lcsk_9:
	v_bfe_u32 v49, v37, 16, 7
	v_cndmask_b32_e64 v49, v49, v24, s[48:49]
	v_lshlrev_b32_e32 v49, 2, v49
	s_waitcnt vmcnt(12)
	s_cmp_eq_u64 s[48:49], exec
	s_cbranch_scc1 .Lcsk_10
	ds_add_u32 v49, v72 offset:1024
	ds_add_u32 v49, v73 offset:1792
	ds_add_rtn_u32 v73, v49, v25 offset:2560
	ds_read_b32 v74, v49 offset:3328
.Lcsk_10:
	v_bfe_u32 v49, v36, 16, 7
	v_cndmask_b32_e64 v49, v49, v24, s[46:47]
	v_lshlrev_b32_e32 v49, 2, v49
	s_waitcnt vmcnt(11)
	s_cmp_eq_u64 s[46:47], exec
	s_cbranch_scc1 .Lcsk_11
	ds_add_u32 v49, v98 offset:1024
	ds_add_u32 v49, v99 offset:1792
	ds_add_rtn_u32 v71, v49, v25 offset:2560
	ds_read_b32 v72, v49 offset:3328
.Lcsk_11:
	v_bfe_u32 v49, v35, 16, 7
	v_cndmask_b32_e64 v49, v49, v24, s[44:45]
	v_lshlrev_b32_e32 v49, 2, v49
	s_waitcnt vmcnt(10)
	s_cmp_eq_u64 s[44:45], exec
	s_cbranch_scc1 .Lcsk_12
	ds_add_u32 v49, v100 offset:1024
	ds_add_u32 v49, v101 offset:1792
	ds_add_rtn_u32 v69, v49, v25 offset:2560
	ds_read_b32 v70, v49 offset:3328
.Lcsk_12:
	v_bfe_u32 v49, v34, 16, 7
	v_cndmask_b32_e64 v49, v49, v24, s[42:43]
	v_lshlrev_b32_e32 v49, 2, v49
	s_waitcnt vmcnt(9)
	s_cmp_eq_u64 s[42:43], exec
	s_cbranch_scc1 .Lcsk_13
	ds_add_u32 v49, v102 offset:1024
	ds_add_u32 v49, v103 offset:1792
	ds_add_rtn_u32 v67, v49, v25 offset:2560
	ds_read_b32 v68, v49 offset:3328
.Lcsk_13:
	v_bfe_u32 v49, v33, 16, 7
	v_cndmask_b32_e64 v49, v49, v24, s[40:41]
	v_lshlrev_b32_e32 v49, 2, v49
	s_waitcnt vmcnt(8)
	s_cmp_eq_u64 s[40:41], exec
	s_cbranch_scc1 .Lcsk_14
	ds_add_u32 v49, v104 offset:1024
	ds_add_u32 v49, v105 offset:1792
	ds_add_rtn_u32 v65, v49, v25 offset:2560
	ds_read_b32 v66, v49 offset:3328
.Lcsk_14:
	v_bfe_u32 v49, v32, 16, 7
	v_cndmask_b32_e64 v49, v49, v24, s[38:39]
	v_lshlrev_b32_e32 v49, 2, v49
	s_waitcnt vmcnt(7)
	s_cmp_eq_u64 s[38:39], exec
	s_cbranch_scc1 .Lcsk_15
	ds_add_u32 v49, v106 offset:1024
	ds_add_u32 v49, v107 offset:1792
	ds_add_rtn_u32 v63, v49, v25 offset:2560
	ds_read_b32 v64, v49 offset:3328
.Lcsk_15:
	v_bfe_u32 v49, v31, 16, 7
	v_cndmask_b32_e64 v49, v49, v24, s[36:37]
	v_lshlrev_b32_e32 v49, 2, v49
	s_waitcnt vmcnt(6)
	s_cmp_eq_u64 s[36:37], exec
	s_cbranch_scc1 .Lcsk_16
	ds_add_u32 v49, v108 offset:1024
	ds_add_u32 v49, v109 offset:1792
	ds_add_rtn_u32 v61, v49, v25 offset:2560
	ds_read_b32 v62, v49 offset:3328
.Lcsk_16:
	v_bfe_u32 v49, v30, 16, 7
	v_cndmask_b32_e64 v49, v49, v24, s[34:35]
	v_lshlrev_b32_e32 v49, 2, v49
	s_waitcnt vmcnt(5)
	s_cmp_eq_u64 s[34:35], exec
	s_cbranch_scc1 .Lcsk_17
	ds_add_u32 v49, v110 offset:1024
	ds_add_u32 v49, v111 offset:1792
	ds_add_rtn_u32 v59, v49, v25 offset:2560
	ds_read_b32 v60, v49 offset:3328
.Lcsk_17:
	v_bfe_u32 v49, v29, 16, 7
	v_cndmask_b32_e64 v49, v49, v24, s[30:31]
	v_lshlrev_b32_e32 v49, 2, v49
	s_waitcnt vmcnt(4)
	s_cmp_eq_u64 s[30:31], exec
	s_cbranch_scc1 .Lcsk_18
	ds_add_u32 v49, v112 offset:1024
	ds_add_u32 v49, v113 offset:1792
	ds_add_rtn_u32 v57, v49, v25 offset:2560
	ds_read_b32 v58, v49 offset:3328
.Lcsk_18:
	v_bfe_u32 v49, v28, 16, 7
	v_cndmask_b32_e64 v49, v49, v24, s[28:29]
	v_lshlrev_b32_e32 v49, 2, v49
	s_waitcnt vmcnt(3)
	s_cmp_eq_u64 s[28:29], exec
	s_cbranch_scc1 .Lcsk_19
	ds_add_u32 v49, v114 offset:1024
	ds_add_u32 v49, v115 offset:1792
	ds_add_rtn_u32 v54, v49, v25 offset:2560
	ds_read_b32 v56, v49 offset:3328
.Lcsk_19:
	v_bfe_u32 v49, v27, 16, 7
	v_cndmask_b32_e64 v49, v49, v24, s[26:27]
	v_lshlrev_b32_e32 v49, 2, v49
	s_waitcnt vmcnt(2)
	s_cmp_eq_u64 s[26:27], exec
	s_cbranch_scc1 .Lcsk_20
	ds_add_u32 v49, v116 offset:1024
	ds_add_u32 v49, v117 offset:1792
	ds_add_rtn_u32 v51, v49, v25 offset:2560
	ds_read_b32 v52, v49 offset:3328
.Lcsk_20:
	v_bfe_u32 v49, v26, 16, 7
	v_cndmask_b32_e64 v49, v49, v24, s[24:25]
	v_bfe_u32 v53, v2, 16, 7
	v_lshlrev_b32_e32 v50, 2, v49
	v_cndmask_b32_e64 v53, v53, v24, s[22:23]
	s_waitcnt vmcnt(1)
	s_cmp_eq_u64 s[24:25], exec
	s_cbranch_scc1 .Lcsk_21
	ds_add_u32 v50, v118 offset:1024
	ds_add_u32 v50, v119 offset:1792
	ds_add_rtn_u32 v49, v50, v25 offset:2560
.Lcsk_21:
	v_lshlrev_b32_e32 v55, 2, v53
	s_cmp_eq_u64 s[24:25], exec
	s_cbranch_scc1 .Lcsk_22
	ds_read_b32 v50, v50 offset:3328
.Lcsk_22:
	s_waitcnt vmcnt(0)
	s_cmp_eq_u64 s[22:23], exec
	s_cbranch_scc1 .Lcsk_23
	ds_add_u32 v55, v120 offset:1024
	ds_add_u32 v55, v121 offset:1792
	ds_add_rtn_u32 v53, v55, v25 offset:2560
	ds_read_b32 v55, v55 offset:3328
.Lcsk_23:
	v_cmp_ne_u32_e64 s[50:51], -1, v48
	v_cmp_ne_u32_e64 s[46:47], -1, v47
	v_cmp_ne_u32_e64 s[44:45], -1, v46
	v_cmp_ne_u32_e64 s[42:43], -1, v45
	v_cmp_ne_u32_e64 s[40:41], -1, v44
	v_cmp_ne_u32_e64 s[38:39], -1, v43
	v_cmp_ne_u32_e64 s[36:37], -1, v42
	v_cmp_ne_u32_e64 s[34:35], -1, v41
	v_cmp_ne_u32_e64 s[30:31], -1, v40
	v_cmp_ne_u32_e64 s[28:29], -1, v39
	v_cmp_ne_u32_e64 s[26:27], -1, v38
	v_cmp_ne_u32_e64 s[24:25], -1, v37
	v_cmp_ne_u32_e64 s[22:23], -1, v36
	v_cmp_ne_u32_e64 s[18:19], -1, v34
	v_cmp_ne_u32_e64 s[16:17], -1, v33
	v_cmp_ne_u32_e64 s[14:15], -1, v32
	v_cmp_ne_u32_e64 s[12:13], -1, v31
	v_cmp_ne_u32_e64 s[10:11], -1, v30
	v_cmp_ne_u32_e64 s[8:9], -1, v29
	v_cmp_ne_u32_e64 s[6:7], -1, v28
	v_cmp_ne_u32_e64 s[4:5], -1, v27
	v_cmp_ne_u32_e64 s[48:49], -1, v26
	v_cmp_ne_u32_e64 s[0:1], -1, v2
	s_and_saveexec_b64 s[66:67], s[50:51]
	s_cbranch_execnz .LBB2_53
	s_or_b64 exec, exec, s[66:67]
	s_and_saveexec_b64 s[50:51], s[46:47]
	s_cbranch_execnz .LBB2_54

.LBB2_54:
	s_waitcnt lgkmcnt(0)
	v_add3_u32 v94, v95, v94, v12
	v_ashrrev_i32_e32 v95, 31, v94
	v_lshl_add_u64 v[94:95], v[94:95], 2, s[54:55]
	global_store_dword v[94:95], v47, off
	s_or_b64 exec, exec, s[50:51]
	s_and_saveexec_b64 s[46:47], s[44:45]
	s_cbranch_execz .LBB2_32
.LBB2_55:
	s_waitcnt lgkmcnt(0)
	v_add3_u32 v92, v93, v92, v12
	v_ashrrev_i32_e32 v93, 31, v92
	v_lshl_add_u64 v[92:93], v[92:93], 2, s[54:55]
	global_store_dword v[92:93], v46, off
	s_or_b64 exec, exec, s[46:47]
	s_and_saveexec_b64 s[44:45], s[42:43]
	s_cbranch_execz .LBB2_33
.LBB2_56:
	s_waitcnt lgkmcnt(0)
	v_add3_u32 v46, v90, v89, v12
	v_ashrrev_i32_e32 v47, 31, v46
	v_lshl_add_u64 v[46:47], v[46:47], 2, s[54:55]
	global_store_dword v[46:47], v45, off
	s_or_b64 exec, exec, s[44:45]
	s_and_saveexec_b64 s[42:43], s[40:41]
	s_cbranch_execz .LBB2_34
.LBB2_57:
	s_waitcnt lgkmcnt(0)
	v_add3_u32 v46, v88, v87, v12
	v_ashrrev_i32_e32 v47, 31, v46
	v_lshl_add_u64 v[46:47], v[46:47], 2, s[54:55]
	global_store_dword v[46:47], v44, off
	s_or_b64 exec, exec, s[42:43]
	s_and_saveexec_b64 s[40:41], s[38:39]
	s_cbranch_execz .LBB2_35
.LBB2_58:
	s_waitcnt lgkmcnt(0)
	v_add3_u32 v44, v86, v85, v12
	v_ashrrev_i32_e32 v45, 31, v44
	v_lshl_add_u64 v[44:45], v[44:45], 2, s[54:55]
	global_store_dword v[44:45], v43, off
	s_or_b64 exec, exec, s[40:41]
	s_and_saveexec_b64 s[38:39], s[36:37]
	s_cbranch_execz .LBB2_36
.LBB2_59:
	s_waitcnt lgkmcnt(0)
	v_add3_u32 v44, v84, v83, v12
	v_ashrrev_i32_e32 v45, 31, v44
	v_lshl_add_u64 v[44:45], v[44:45], 2, s[54:55]
	global_store_dword v[44:45], v42, off
	s_or_b64 exec, exec, s[38:39]
	s_and_saveexec_b64 s[36:37], s[34:35]
	s_cbranch_execz .LBB2_37
.LBB2_60:
	s_waitcnt lgkmcnt(0)
	v_add3_u32 v42, v82, v81, v12
	v_ashrrev_i32_e32 v43, 31, v42
	v_lshl_add_u64 v[42:43], v[42:43], 2, s[54:55]
	global_store_dword v[42:43], v41, off
	s_or_b64 exec, exec, s[36:37]
	s_and_saveexec_b64 s[34:35], s[30:31]
	s_cbranch_execz .LBB2_38
.LBB2_61:
	s_waitcnt lgkmcnt(0)
	v_add3_u32 v42, v80, v79, v12
	v_ashrrev_i32_e32 v43, 31, v42
	v_lshl_add_u64 v[42:43], v[42:43], 2, s[54:55]
	global_store_dword v[42:43], v40, off
	s_or_b64 exec, exec, s[34:35]
	s_and_saveexec_b64 s[30:31], s[28:29]
	s_cbranch_execz .LBB2_39
.LBB2_62:
	s_waitcnt lgkmcnt(0)
	v_add3_u32 v40, v78, v77, v12
	v_ashrrev_i32_e32 v41, 31, v40
	v_lshl_add_u64 v[40:41], v[40:41], 2, s[54:55]
	global_store_dword v[40:41], v39, off
	s_or_b64 exec, exec, s[30:31]
	s_and_saveexec_b64 s[28:29], s[26:27]
	s_cbranch_execz .LBB2_40
.LBB2_63:
	s_waitcnt lgkmcnt(0)
	v_add3_u32 v40, v76, v75, v12
	v_ashrrev_i32_e32 v41, 31, v40
	v_lshl_add_u64 v[40:41], v[40:41], 2, s[54:55]
	global_store_dword v[40:41], v38, off
	s_or_b64 exec, exec, s[28:29]
	s_and_saveexec_b64 s[26:27], s[24:25]
	s_cbranch_execz .LBB2_41
.LBB2_64:
	s_waitcnt lgkmcnt(0)
	v_add3_u32 v38, v74, v73, v12
	v_ashrrev_i32_e32 v39, 31, v38
	v_lshl_add_u64 v[38:39], v[38:39], 2, s[54:55]
	global_store_dword v[38:39], v37, off
	s_or_b64 exec, exec, s[26:27]
	s_and_saveexec_b64 s[24:25], s[22:23]
	s_cbranch_execz .LBB2_42
.LBB2_65:
	s_waitcnt lgkmcnt(0)
	v_add3_u32 v38, v72, v71, v12
	v_ashrrev_i32_e32 v39, 31, v38
	v_lshl_add_u64 v[38:39], v[38:39], 2, s[54:55]
	global_store_dword v[38:39], v36, off
	s_or_b64 exec, exec, s[24:25]
	s_and_saveexec_b64 s[22:23], s[20:21]
	s_cbranch_execz .LBB2_43
.LBB2_66:
	s_waitcnt lgkmcnt(0)
	v_add3_u32 v36, v70, v69, v12
	v_ashrrev_i32_e32 v37, 31, v36
	v_lshl_add_u64 v[36:37], v[36:37], 2, s[54:55]
	global_store_dword v[36:37], v35, off
	s_or_b64 exec, exec, s[22:23]
	s_and_saveexec_b64 s[20:21], s[18:19]
	s_cbranch_execz .LBB2_44
.LBB2_67:
	s_waitcnt lgkmcnt(0)
	v_add3_u32 v36, v68, v67, v12
	v_ashrrev_i32_e32 v37, 31, v36
	v_lshl_add_u64 v[36:37], v[36:37], 2, s[54:55]
	global_store_dword v[36:37], v34, off
	s_or_b64 exec, exec, s[20:21]
	s_and_saveexec_b64 s[18:19], s[16:17]
	s_cbranch_execz .LBB2_45
.LBB2_68:
	s_waitcnt lgkmcnt(0)
	v_add3_u32 v34, v66, v65, v12
	v_ashrrev_i32_e32 v35, 31, v34
	v_lshl_add_u64 v[34:35], v[34:35], 2, s[54:55]
	global_store_dword v[34:35], v33, off
	s_or_b64 exec, exec, s[18:19]
	s_and_saveexec_b64 s[16:17], s[14:15]
	s_cbranch_execz .LBB2_46
.LBB2_69:
	s_waitcnt lgkmcnt(0)
	v_add3_u32 v34, v64, v63, v12
	v_ashrrev_i32_e32 v35, 31, v34
	v_lshl_add_u64 v[34:35], v[34:35], 2, s[54:55]
	global_store_dword v[34:35], v32, off
	s_or_b64 exec, exec, s[16:17]
	s_and_saveexec_b64 s[14:15], s[12:13]
	s_cbranch_execz .LBB2_47
.LBB2_70:
	s_waitcnt lgkmcnt(0)
	v_add3_u32 v32, v62, v61, v12
	v_ashrrev_i32_e32 v33, 31, v32
	v_lshl_add_u64 v[32:33], v[32:33], 2, s[54:55]
	global_store_dword v[32:33], v31, off
	s_or_b64 exec, exec, s[14:15]
	s_and_saveexec_b64 s[12:13], s[10:11]
	s_cbranch_execz .LBB2_48
.LBB2_71:
	s_waitcnt lgkmcnt(0)
	v_add3_u32 v32, v60, v59, v12
	v_ashrrev_i32_e32 v33, 31, v32
	v_lshl_add_u64 v[32:33], v[32:33], 2, s[54:55]
	global_store_dword v[32:33], v30, off
	s_or_b64 exec, exec, s[12:13]
	s_and_saveexec_b64 s[10:11], s[8:9]
	s_cbranch_execz .LBB2_49
.LBB2_72:
	s_waitcnt lgkmcnt(0)
	v_add3_u32 v30, v58, v57, v12
	v_ashrrev_i32_e32 v31, 31, v30
	v_lshl_add_u64 v[30:31], v[30:31], 2, s[54:55]
	global_store_dword v[30:31], v29, off
	s_or_b64 exec, exec, s[10:11]
	s_and_saveexec_b64 s[8:9], s[6:7]
	s_cbranch_execz .LBB2_50
.LBB2_73:
	s_waitcnt lgkmcnt(0)
	v_add3_u32 v30, v56, v54, v12
	v_ashrrev_i32_e32 v31, 31, v30
	v_lshl_add_u64 v[30:31], v[30:31], 2, s[54:55]
	global_store_dword v[30:31], v28, off
	s_or_b64 exec, exec, s[8:9]
	s_and_saveexec_b64 s[6:7], s[4:5]
	s_cbranch_execz .LBB2_51
.LBB2_74:
	s_waitcnt lgkmcnt(0)
	v_add3_u32 v28, v52, v51, v12
	v_ashrrev_i32_e32 v29, 31, v28
	v_lshl_add_u64 v[28:29], v[28:29], 2, s[54:55]
	global_store_dword v[28:29], v27, off
	s_or_b64 exec, exec, s[6:7]
	s_and_saveexec_b64 s[4:5], s[48:49]
	s_cbranch_execz .LBB2_52
.LBB2_75:
	s_waitcnt lgkmcnt(0)
	v_add3_u32 v28, v50, v49, v12
	v_ashrrev_i32_e32 v29, 31, v28
	v_lshl_add_u64 v[28:29], v[28:29], 2, s[54:55]
	global_store_dword v[28:29], v26, off
	s_or_b64 exec, exec, s[4:5]
	s_and_saveexec_b64 s[4:5], s[0:1]
	s_cbranch_execz .LBB2_28
